# MoE split gate/up and down schedulers: the expert-table search for the next unit resumes from the previous unit's expert (row tiles only grow within a workgroup) instead of scanning the LDS table from
# baseline (speedup 1.0000x reference)
; #define G_STAGE2(bufoff, gbase, v0, v1) do { \
;         __builtin_amdgcn_global_load_lds((const unsigned*)((const char*)(gbase) + (v0)), (LAS unsigned*)(lds + (bufoff) + ldsw), 16, 0, 0); \
;         __builtin_amdgcn_global_load_lds((const unsigned*)((const char*)(gbase) + (v1)), (LAS unsigned*)(lds + (bufoff) + ldsw + 8192), 16, 0, 0); } while (0)
; #define G_WAIT_V(n) asm volatile("s_waitcnt vmcnt(" #n ")" ::: "memory")
; #define G_BAR __builtin_amdgcn_s_barrier()
; __device__ __forceinline__ int moe_expert_of(const LAS int* tb, int rt) { int e = 0; while (tb[e + 1] <= rt) ++e; return e; }
; template <bool PERM, class Epi, class Sched>
; __device__ __forceinline__ void gemm_phase(LAS unsigned char* lds, const Sched& S, const Epi& E) {
;     ...
;     G_STAGE2(G_SB(0, 0), cB, vb0, vb1); G_STAGE2(G_SA(0, 0), cA, va00, va01); G_STAGE2(G_SB(0, 1), cB + hsB, vb0, vb1); G_STAGE2(G_SA(0, 1), cA, va10, va11);
;     if (wr == 1) G_BAR;
;     G_WAIT_V(4); G_BAR;
;     G_STAGE2(G_SB(1, 0), cB + kstep, vb0, vb1); G_STAGE2(G_SA(1, 0), cA + kstep, va00, va01); G_STAGE2(G_SB(1, 1), cB + hsB + kstep, vb0, vb1);
;     G_WAIT_V(6); G_BAR;
;     __device__ __forceinline__ bool next(int i, gm::GUnit& u) const {
;         constexpr int NCT = GUPASS ? 8 : 4;
;         const int L = i * G + c, rt = nfull + L / NCT, ct = L % NCT;
;         if (rt >= tb[32]) return false;
;         const int e = moe_expert_of(tb, rt);
;         u.pm = rt; u.pn = ct; u.e = e; u.lda = 2048; u.ldb = 2048; u.nt = 16; u.aux = (unsigned)(rt - nfull) * (256u * 2048u);
.LBB0_1738:
	s_mov_b32 s100, 0
	s_and_b32 s2, s1, 3
	v_and_b32_e32 v6, 48, v1
	v_lshlrev_b32_e32 v7, 6, v1
	s_movk_i32 s1, 0x3c0
	v_lshlrev_b32_e32 v1, 2, v1
	v_lshl_add_u64 v[2:3], s[28:29], 0, v[146:147]
	s_lshl_b32 s62, s0, 6
	s_lshl_b32 s0, s0, 13
	v_and_or_b32 v6, v7, s1, v6
	v_and_b32_e32 v1, 32, v1
	v_bitop3_b32 v7, v6, s0, v1 bitop3:0xde
	s_lshl_b32 s0, s2, 12
	v_lshl_add_u64 v[2:3], v[2:3], 0, s[34:35]
	s_add_i32 m0, s41, 0x18000
	v_mov_b32_e32 v189, v147
	v_bitop3_b32 v1, v6, s0, v1 bitop3:0xde
	s_waitcnt vmcnt(4)
	s_barrier
	global_load_lds_dwordx4 v[2:3], off
	s_add_i32 m0, s41, 0x1a000
	v_readlane_b32 s0, v255, 11
	v_lshl_add_u64 v[4:5], s[28:29], 0, v[188:189]
	v_readlane_b32 s1, v255, 12
	s_add_u32 s50, s0, 0x13f16180
	v_mov_b32_e32 v181, v147
	v_lshl_add_u64 v[2:3], v[4:5], 0, s[34:35]
	s_addc_u32 s51, s1, 0
	s_add_i32 s63, s41, 0x8000
	s_add_i32 s71, s41, 0xa000
	v_mov_b32_e32 v183, v147
	global_load_lds_dwordx4 v[2:3], off
	v_lshl_add_u64 v[2:3], s[50:51], 0, v[180:181]
	s_mov_b32 m0, s63
	s_add_u32 s0, s28, 0x40080
	global_load_lds_dwordx4 v[2:3], off
	v_lshl_add_u64 v[2:3], s[50:51], 0, v[182:183]
	s_mov_b32 m0, s71
	s_addc_u32 s1, s29, 0
	global_load_lds_dwordx4 v[2:3], off
	v_lshl_add_u64 v[2:3], s[0:1], 0, v[146:147]
	s_add_i32 m0, s41, 0x1c000
	s_lshl_b32 s72, s2, 4
	global_load_lds_dwordx4 v[2:3], off
	v_lshl_add_u64 v[2:3], s[0:1], 0, v[188:189]
	s_add_i32 m0, s41, 0x1e000
	s_mov_b32 s73, 0
	global_load_lds_dwordx4 v[2:3], off
	s_waitcnt vmcnt(6)
	v_add_u32_e32 v199, 0, v7
	v_readlane_b32 s1, v253, 37
	v_readlane_b32 s0, v253, 46
	s_mov_b64 s[54:55], s[28:29]
	s_barrier
	s_branch .LBB0_1740

;     __device__ __forceinline__ int* rtok() const { return (int*)(ws + WS_RTOK); }
; __device__ __forceinline__ int moe_expert_of(const LAS int* tb, int rt) { int e = 0; while (tb[e + 1] <= rt) ++e; return e; }
;     __device__ __forceinline__ bool next(int i, gm::GUnit& u) const {
;         constexpr int NCT = GUPASS ? 8 : 4;
;         const int L = i * G + c, rt = nfull + L / NCT, ct = L % NCT;
;         if (rt >= tb[32]) return false;
;         const int e = moe_expert_of(tb, rt);
;         u.pm = rt; u.pn = ct; u.e = e; u.lda = 2048; u.ldb = 2048; u.nt = 16; u.aux = (unsigned)(rt - nfull) * (256u * 2048u);
;         if (GUPASS) { u.sub = ct; u.A = A; u.gidx = rtok + (size_t)rt * 256; u.B = W + ((size_t)e * 2048 + ct * 256) * 2048; }
;         else { u.sub = 8 + ct; u.A = A + u.aux; u.gidx = nullptr; u.B = W + ((size_t)e * 1024 + ct * 256) * 2048; }
.LBB0_1740:
	s_add_i32 s73, s73, 1
	s_mul_i32 s2, s73, s96
	v_readlane_b32 s8, v254, 62
	s_add_i32 s2, s2, s8
	v_readlane_b32 s8, v254, 26
	s_ashr_i32 s7, s2, 31
	s_lshr_b32 s7, s7, 29
	v_mov_b32_e32 v2, s8
	ds_read_b32 v2, v2
	s_add_i32 s7, s2, s7
	s_ashr_i32 s7, s7, 3
	s_add_i32 s8, s7, s64
	v_readlane_b32 s9, v254, 63
	s_waitcnt lgkmcnt(0)
	v_cmp_ge_i32_e64 s[42:43], s8, v2
	v_cmp_lt_i32_e64 s[44:45], s8, v2
	s_and_b64 vcc, exec, s[42:43]
	s_cbranch_vccnz .LBB0_1744
	s_lshl_b32 s9, s100, 2
	s_add_i32 s9, s9, 0x23044
	s_add_i32 s76, s100, -1
.LBB0_1742:
	v_mov_b32_e32 v2, s9
	ds_read_b32 v2, v2
	s_add_i32 s76, s76, 1
	s_add_i32 s9, s9, 4
	s_waitcnt lgkmcnt(0)
	v_cmp_ge_i32_e32 vcc, s8, v2
	s_cbranch_vccnz .LBB0_1742
	s_mov_b32 s100, s76
	s_lshl_b32 s9, s7, 3
	s_sub_i32 s78, s2, s9
	s_ashr_i32 s9, s8, 31
	s_lshl_b32 s79, s7, 19
	s_lshl_b64 s[8:9], s[8:9], 10
	s_add_u32 s52, s46, s8
	s_addc_u32 s53, s47, s9
	s_lshl_b32 s8, s78, 8
	s_ashr_i32 s9, s8, 31
	s_lshl_b64 s[22:23], s[76:77], 22
	s_lshl_b64 s[8:9], s[8:9], 11
	s_add_u32 s2, s74, s22
	s_addc_u32 s7, s75, s23
	s_add_u32 s54, s2, s8
	s_addc_u32 s55, s7, s9

; #define G_STAGE2(bufoff, gbase, v0, v1) do { \
;         __builtin_amdgcn_global_load_lds((const unsigned*)((const char*)(gbase) + (v0)), (LAS unsigned*)(lds + (bufoff) + ldsw), 16, 0, 0); \
;         __builtin_amdgcn_global_load_lds((const unsigned*)((const char*)(gbase) + (v1)), (LAS unsigned*)(lds + (bufoff) + ldsw + 8192), 16, 0, 0); } while (0)
; #define G_WAIT_V(n) asm volatile("s_waitcnt vmcnt(" #n ")" ::: "memory")
; #define G_BAR __builtin_amdgcn_s_barrier()
; __device__ __forceinline__ int moe_expert_of(const LAS int* tb, int rt) { int e = 0; while (tb[e + 1] <= rt) ++e; return e; }
; template <bool PERM, class Epi, class Sched>
; __device__ __forceinline__ void gemm_phase(LAS unsigned char* lds, const Sched& S, const Epi& E) {
;     ...
;     G_STAGE2(G_SB(0, 0), cB, vb0, vb1); G_STAGE2(G_SA(0, 0), cA, va00, va01); G_STAGE2(G_SB(0, 1), cB + hsB, vb0, vb1); G_STAGE2(G_SA(0, 1), cA, va10, va11);
;     if (wr == 1) G_BAR;
;     G_WAIT_V(4); G_BAR;
;     G_STAGE2(G_SB(1, 0), cB + kstep, vb0, vb1); G_STAGE2(G_SA(1, 0), cA + kstep, va00, va01); G_STAGE2(G_SB(1, 1), cB + hsB + kstep, vb0, vb1);
;     G_WAIT_V(6); G_BAR;
;     __device__ __forceinline__ bool next(int i, gm::GUnit& u) const {
;         constexpr int NCT = GUPASS ? 8 : 4;
;         const int L = i * G + c, rt = nfull + L / NCT, ct = L % NCT;
;         if (rt >= tb[32]) return false;
;         const int e = moe_expert_of(tb, rt);
;         u.pm = rt; u.pn = ct; u.e = e; u.lda = 2048; u.ldb = 2048; u.nt = 16; u.aux = (unsigned)(rt - nfull) * (256u * 2048u);
.LBB0_1846:
	s_mov_b32 s101, 0
	v_lshl_add_u64 v[2:3], s[18:19], 0, v[146:147]
	v_mov_b32_e32 v189, v147
	v_and_b32_e32 v10, 48, v1
	v_lshlrev_b32_e32 v11, 6, v1
	s_movk_i32 s28, 0x3c0
	v_lshlrev_b32_e32 v1, 2, v1
	v_lshl_add_u64 v[4:5], s[18:19], 0, v[188:189]
	v_mov_b32_e32 v181, v147
	s_and_b32 s7, s7, 3
	s_lshl_b32 s55, s2, 6
	s_lshl_b32 s2, s2, 13
	v_and_or_b32 v10, v11, s28, v10
	v_and_b32_e32 v1, 32, v1
	v_lshl_add_u64 v[2:3], v[2:3], 0, s[34:35]
	s_add_i32 m0, s24, 0x18000
	v_lshl_add_u64 v[6:7], s[8:9], 0, v[180:181]
	v_mov_b32_e32 v183, v147
	v_bitop3_b32 v11, v10, s2, v1 bitop3:0xde
	s_lshl_b32 s56, s7, 5
	s_lshl_b32 s2, s7, 12
	s_waitcnt vmcnt(4)
	s_barrier
	global_load_lds_dwordx4 v[2:3], off
	v_lshl_add_u64 v[2:3], v[4:5], 0, s[34:35]
	s_add_i32 m0, s24, 0x1a000
	s_add_i32 s57, s24, 0x8000
	s_add_i32 s60, s24, 0xa000
	v_lshl_add_u64 v[8:9], s[8:9], 0, v[182:183]
	global_load_lds_dwordx4 v[2:3], off
	v_lshl_add_u64 v[2:3], v[6:7], 0, s[34:35]
	s_mov_b32 m0, s57
	s_add_u32 s28, s18, 0x40080
	global_load_lds_dwordx4 v[2:3], off
	v_lshl_add_u64 v[2:3], v[8:9], 0, s[34:35]
	s_mov_b32 m0, s60
	s_addc_u32 s29, s19, 0
	global_load_lds_dwordx4 v[2:3], off
	v_lshl_add_u64 v[2:3], s[28:29], 0, v[146:147]
	s_add_i32 m0, s24, 0x1c000
	v_bitop3_b32 v1, v10, s2, v1 bitop3:0xde
	global_load_lds_dwordx4 v[2:3], off
	v_lshl_add_u64 v[2:3], s[28:29], 0, v[188:189]
	s_add_i32 m0, s24, 0x1e000
	s_lshl_b32 s61, s7, 4
	global_load_lds_dwordx4 v[2:3], off
	s_waitcnt vmcnt(6)
	s_mov_b32 s62, 0
	v_add_u32_e32 v192, 0, v11
	v_readlane_b32 s7, v253, 50
	v_readlane_b32 s2, v253, 49
	s_mov_b64 s[48:49], s[8:9]
	s_mov_b64 s[50:51], s[18:19]
	s_barrier
	s_branch .LBB0_1848

;     __device__ __forceinline__ int* rtok() const { return (int*)(ws + WS_RTOK); }
; __device__ __forceinline__ int moe_expert_of(const LAS int* tb, int rt) { int e = 0; while (tb[e + 1] <= rt) ++e; return e; }
;     __device__ __forceinline__ bool next(int i, gm::GUnit& u) const {
;         constexpr int NCT = GUPASS ? 8 : 4;
;         const int L = i * G + c, rt = nfull + L / NCT, ct = L % NCT;
;         if (rt >= tb[32]) return false;
;         const int e = moe_expert_of(tb, rt);
;         u.pm = rt; u.pn = ct; u.e = e; u.lda = 2048; u.ldb = 2048; u.nt = 16; u.aux = (unsigned)(rt - nfull) * (256u * 2048u);
;         if (GUPASS) { u.sub = ct; u.A = A; u.gidx = rtok + (size_t)rt * 256; u.B = W + ((size_t)e * 2048 + ct * 256) * 2048; }
;         else { u.sub = 8 + ct; u.A = A + u.aux; u.gidx = nullptr; u.B = W + ((size_t)e * 1024 + ct * 256) * 2048; }
.LBB0_1848:
	s_add_i32 s62, s62, 1
	s_mul_i32 s29, s62, s96
	v_readlane_b32 s28, v253, 40
	v_readlane_b32 s40, v254, 26
	s_add_i32 s29, s29, s28
	s_ashr_i32 s28, s29, 31
	v_mov_b32_e32 v2, s40
	ds_read_b32 v2, v2
	s_lshr_b32 s28, s28, 30
	s_add_i32 s28, s29, s28
	s_ashr_i32 s82, s28, 2
	s_add_i32 s28, s82, s64
	s_waitcnt lgkmcnt(0)
	v_cmp_ge_i32_e64 s[40:41], s28, v2
	v_cmp_lt_i32_e64 s[42:43], s28, v2
	s_and_b64 vcc, exec, s[40:41]
	s_cbranch_vccnz .LBB0_1852
	s_lshl_b32 s48, s101, 2
	s_add_i32 s48, s48, 0x23044
	s_add_i32 s76, s101, -1
.LBB0_1850:
	v_mov_b32_e32 v2, s48
	ds_read_b32 v2, v2
	s_add_i32 s76, s76, 1
	s_add_i32 s48, s48, 4
	s_waitcnt lgkmcnt(0)
	v_cmp_ge_i32_e32 vcc, s28, v2
	s_cbranch_vccnz .LBB0_1850
	s_mov_b32 s101, s76
	s_lshl_b32 s48, s82, 2
	s_sub_i32 s74, s29, s48
	s_lshl_b32 s78, s82, 19
	s_add_i32 s75, s74, 8
	s_add_u32 s48, s65, s78
	s_addc_u32 s49, s66, 0
	s_lshl_b32 s50, s74, 8
	s_ashr_i32 s51, s50, 31
	s_lshl_b64 s[82:83], s[76:77], 21
	s_lshl_b64 s[50:51], s[50:51], 11
	s_add_u32 s29, s58, s82
	s_addc_u32 s79, s59, s83
	s_add_u32 s50, s29, s50
	s_addc_u32 s51, s79, s51
	s_mov_b32 s79, s28
